# speedup vs baseline: 1.0234x; 1.0097x over previous
_Z11attn_kernelPKDF16_S0_S0_PDF16_:
	v_readfirstlane_b32 s50, v0
	s_lshr_b32 s50, s50, 7
	s_and_b32 s6, s2, 3
	s_cmpk_gt_u32 s2, 0xdf
	s_mul_i32 s6, s6, 7
	s_cbranch_scc0 .LBB1_2
	s_lshr_b32 s3, s2, 3
	s_sub_i32 s4, s3, 28
	s_lshl_b32 s3, s4, 1
	s_add_i32 s3, s3, s6
	s_add_i32 s28, s3, 1
	s_cmp_eq_u32 s4, 3
	s_cselect_b32 s30, -1, 3
	s_movk_i32 s14, 0x300
	s_cbranch_execz .LBB1_3
	s_branch .LBB1_4

.LBB1_27:
	s_add_i32 s25, s45, s24
	s_add_i32 s2, s44, s40
	s_add_i32 s3, s25, 2
	s_mov_b32 s51, s3
	s_cmp_lt_i32 s3, s50
	s_mov_b32 s3, m0
	s_mov_b32 m0, s2
	s_nop 0
	global_load_lds_dwordx4 v211, s[18:19]
	s_mov_b32 m0, s3
	s_cbranch_scc1 .LBB1_29
	s_cmp_gt_i32 s51, s50
	s_cbranch_scc1 .Lmfill_0a
	v_add_u32_e32 v60, 0xffffffa5, v201
	v_add_u32_e32 v59, 0xffffff85, v201
	v_cmp_le_i32_e32 vcc, v60, v204
	s_nop 1
	v_cndmask_b32_e32 v82, v205, v82, vcc
	v_cmp_lt_i32_e32 vcc, v59, v204
	s_nop 1
	v_cndmask_b32_e32 v99, v205, v99, vcc
	v_cmp_le_i32_e32 vcc, v59, v204
	v_add_u32_e32 v59, 0xffffffa6, v201
	s_nop 0
	v_cndmask_b32_e32 v98, v205, v98, vcc
	v_cmp_le_i32_e32 vcc, v59, v204
	v_add_u32_e32 v59, 0xffffff87, v201
	s_nop 0
	v_cndmask_b32_e32 v83, v205, v83, vcc
	v_cmp_le_i32_e32 vcc, v59, v204
	v_add_u32_e32 v59, 0xffffffa7, v201
	s_nop 0
	v_cndmask_b32_e32 v100, v205, v100, vcc
	v_cmp_le_i32_e32 vcc, v59, v204
	v_add_u32_e32 v59, 0xffffff88, v201
	s_nop 0
	v_cndmask_b32_e32 v84, v205, v84, vcc
	v_cmp_le_i32_e32 vcc, v59, v204
	v_add_u32_e32 v59, 0xffffffa8, v201
	s_nop 0
	v_cndmask_b32_e32 v101, v205, v101, vcc
	v_cmp_le_i32_e32 vcc, v59, v204
	v_add_u32_e32 v59, 0xffffff8d, v201
	s_nop 0
	v_cndmask_b32_e32 v85, v205, v85, vcc
	v_cmp_le_i32_e32 vcc, v59, v204
	v_add_u32_e32 v59, 0xffffffad, v201
	s_nop 0
	v_cndmask_b32_e32 v102, v205, v102, vcc
	v_cmp_le_i32_e32 vcc, v59, v204
	v_add_u32_e32 v59, 0xffffff8e, v201
	s_nop 0
	v_cndmask_b32_e32 v86, v205, v86, vcc
	v_cmp_le_i32_e32 vcc, v59, v204
	v_add_u32_e32 v59, 0xffffffae, v201
	s_nop 0
	v_cndmask_b32_e32 v103, v205, v103, vcc
	v_cmp_le_i32_e32 vcc, v59, v204
	v_add_u32_e32 v59, 0xffffff8f, v201
	s_nop 0
	v_cndmask_b32_e32 v87, v205, v87, vcc
	v_cmp_le_i32_e32 vcc, v59, v204
	v_add_u32_e32 v59, 0xffffffaf, v201
	s_nop 0
	v_cndmask_b32_e32 v104, v205, v104, vcc
	v_cmp_le_i32_e32 vcc, v59, v204
	v_add_u32_e32 v59, 0xffffff90, v201
	s_nop 0
	v_cndmask_b32_e32 v88, v205, v88, vcc
	v_cmp_le_i32_e32 vcc, v59, v204
	v_add_u32_e32 v59, 0xffffffb0, v201
	s_nop 0
	v_cndmask_b32_e32 v105, v205, v105, vcc
	v_cmp_le_i32_e32 vcc, v59, v204
	v_add_u32_e32 v59, 0xffffff95, v201
	s_nop 0
	v_cndmask_b32_e32 v89, v205, v89, vcc
	v_cmp_le_i32_e32 vcc, v59, v204
	v_add_u32_e32 v59, 0xffffffb5, v201
	s_nop 0
	v_cndmask_b32_e32 v106, v205, v106, vcc
	v_cmp_le_i32_e32 vcc, v59, v204
	v_add_u32_e32 v59, 0xffffff96, v201
	s_nop 0
	v_cndmask_b32_e32 v90, v205, v90, vcc
	v_cmp_le_i32_e32 vcc, v59, v204
	v_add_u32_e32 v59, 0xffffffb6, v201
	s_nop 0
	v_cndmask_b32_e32 v107, v205, v107, vcc
	v_cmp_le_i32_e32 vcc, v59, v204
	v_add_u32_e32 v59, 0xffffff97, v201
	s_nop 0
	v_cndmask_b32_e32 v91, v205, v91, vcc
	v_cmp_le_i32_e32 vcc, v59, v204
	v_add_u32_e32 v59, 0xffffffb7, v201
	s_nop 0
	v_cndmask_b32_e32 v108, v205, v108, vcc
	v_cmp_le_i32_e32 vcc, v59, v204
	v_add_u32_e32 v59, 0xffffff98, v201
	s_nop 0
	v_cndmask_b32_e32 v92, v205, v92, vcc
	v_cmp_le_i32_e32 vcc, v59, v204
	v_add_u32_e32 v59, 0xffffffb8, v201
	s_nop 0
	v_cndmask_b32_e32 v109, v205, v109, vcc
	v_cmp_le_i32_e32 vcc, v59, v204
	v_add_u32_e32 v59, 0xffffff9d, v201
	s_nop 0
	v_cndmask_b32_e32 v93, v205, v93, vcc
	v_cmp_le_i32_e32 vcc, v59, v204
	v_add_u32_e32 v59, 0xffffffbd, v201
	s_nop 0
	v_cndmask_b32_e32 v110, v205, v110, vcc
	v_cmp_le_i32_e32 vcc, v59, v204
	v_add_u32_e32 v59, 0xffffff9e, v201
	s_nop 0
	v_cndmask_b32_e32 v94, v205, v94, vcc
	v_cmp_le_i32_e32 vcc, v59, v204
	v_add_u32_e32 v59, 0xffffffbe, v201
	s_nop 0
	v_cndmask_b32_e32 v111, v205, v111, vcc
	v_cmp_le_i32_e32 vcc, v59, v204
	v_add_u32_e32 v59, 0xffffff9f, v201
	s_nop 0
	v_cndmask_b32_e32 v95, v205, v95, vcc
	v_cmp_le_i32_e32 vcc, v59, v204
	v_add_u32_e32 v59, 0xffffffbf, v201
	s_nop 0
	v_cndmask_b32_e32 v112, v205, v112, vcc
	v_cmp_le_i32_e32 vcc, v59, v204
	v_add_u32_e32 v59, 0xffffffa0, v201
	s_nop 0
	v_cndmask_b32_e32 v96, v205, v96, vcc
	v_cmp_le_i32_e32 vcc, v59, v204
	v_subrev_u32_e32 v59, 64, v201
	s_nop 0
	v_cndmask_b32_e32 v113, v205, v113, vcc
	v_cmp_le_i32_e32 vcc, v59, v204
	s_nop 1
	v_cndmask_b32_e32 v97, v205, v97, vcc

.LBB1_38:
	s_add_i32 s25, s25, 3
	s_cmp_lt_i32 s25, s50
	s_cbranch_scc1 .LBB1_40
	s_cmp_gt_i32 s25, s50
	s_cbranch_scc1 .Lmfill_0b
	v_subrev_u32_e32 v92, 27, v201
	v_subrev_u32_e32 v91, 59, v201
	v_cmp_le_u32_e32 vcc, v92, v204
	s_nop 1
	v_cndmask_b32_e32 v50, v205, v50, vcc
	v_cmp_lt_u32_e32 vcc, v91, v204
	s_nop 1
	v_cndmask_b32_e32 v67, v205, v67, vcc
	v_cmp_le_u32_e32 vcc, v91, v204
	v_subrev_u32_e32 v91, 26, v201
	s_nop 0
	v_cndmask_b32_e32 v66, v205, v66, vcc
	v_cmp_le_u32_e32 vcc, v91, v204
	v_subrev_u32_e32 v91, 57, v201
	s_nop 0
	v_cndmask_b32_e32 v51, v205, v51, vcc
	v_cmp_le_u32_e32 vcc, v91, v204
	v_subrev_u32_e32 v91, 25, v201
	s_nop 0
	v_cndmask_b32_e32 v68, v205, v68, vcc
	v_cmp_le_u32_e32 vcc, v91, v204
	v_subrev_u32_e32 v91, 56, v201
	s_nop 0
	v_cndmask_b32_e32 v52, v205, v52, vcc
	v_cmp_le_u32_e32 vcc, v91, v204
	v_subrev_u32_e32 v91, 24, v201
	s_nop 0
	v_cndmask_b32_e32 v69, v205, v69, vcc
	v_cmp_le_u32_e32 vcc, v91, v204
	v_subrev_u32_e32 v91, 51, v201
	s_nop 0
	v_cndmask_b32_e32 v53, v205, v53, vcc
	v_cmp_le_u32_e32 vcc, v91, v204
	v_subrev_u32_e32 v91, 19, v201
	s_nop 0
	v_cndmask_b32_e32 v70, v205, v70, vcc
	v_cmp_le_u32_e32 vcc, v91, v204
	v_subrev_u32_e32 v91, 50, v201
	s_nop 0
	v_cndmask_b32_e32 v54, v205, v54, vcc
	v_cmp_le_u32_e32 vcc, v91, v204
	v_subrev_u32_e32 v91, 18, v201
	s_nop 0
	v_cndmask_b32_e32 v71, v205, v71, vcc
	v_cmp_le_u32_e32 vcc, v91, v204
	v_subrev_u32_e32 v91, 49, v201
	s_nop 0
	v_cndmask_b32_e32 v55, v205, v55, vcc
	v_cmp_le_u32_e32 vcc, v91, v204
	v_subrev_u32_e32 v91, 17, v201
	s_nop 0
	v_cndmask_b32_e32 v72, v205, v72, vcc
	v_cmp_le_u32_e32 vcc, v91, v204
	v_subrev_u32_e32 v91, 48, v201
	s_nop 0
	v_cndmask_b32_e32 v56, v205, v56, vcc
	v_cmp_le_u32_e32 vcc, v91, v204
	v_add_u32_e32 v91, -16, v201
	s_nop 0
	v_cndmask_b32_e32 v73, v205, v73, vcc
	v_cmp_le_u32_e32 vcc, v91, v204
	v_subrev_u32_e32 v91, 43, v201
	s_nop 0
	v_cndmask_b32_e32 v57, v205, v57, vcc
	v_cmp_le_u32_e32 vcc, v91, v204
	v_add_u32_e32 v91, -11, v201
	s_nop 0
	v_cndmask_b32_e32 v74, v205, v74, vcc
	v_cmp_le_u32_e32 vcc, v91, v204
	v_subrev_u32_e32 v91, 42, v201
	s_nop 0
	v_cndmask_b32_e32 v58, v205, v58, vcc
	v_cmp_le_u32_e32 vcc, v91, v204
	v_add_u32_e32 v91, -10, v201
	s_nop 0
	v_cndmask_b32_e32 v75, v205, v75, vcc
	v_cmp_le_u32_e32 vcc, v91, v204
	v_subrev_u32_e32 v91, 41, v201
	s_nop 0
	v_cndmask_b32_e32 v59, v205, v59, vcc
	v_cmp_le_u32_e32 vcc, v91, v204
	v_add_u32_e32 v91, -9, v201
	s_nop 0
	v_cndmask_b32_e32 v76, v205, v76, vcc
	v_cmp_le_u32_e32 vcc, v91, v204
	v_subrev_u32_e32 v91, 40, v201
	s_nop 0
	v_cndmask_b32_e32 v60, v205, v60, vcc
	v_cmp_le_u32_e32 vcc, v91, v204
	v_add_u32_e32 v91, -8, v201
	s_nop 0
	v_cndmask_b32_e32 v77, v205, v77, vcc
	v_cmp_le_u32_e32 vcc, v91, v204
	v_subrev_u32_e32 v91, 35, v201
	s_nop 0
	v_cndmask_b32_e32 v61, v205, v61, vcc
	v_cmp_le_u32_e32 vcc, v91, v204
	v_add_u32_e32 v91, -3, v201
	s_nop 0
	v_cndmask_b32_e32 v78, v205, v78, vcc
	v_cmp_le_u32_e32 vcc, v91, v204
	v_subrev_u32_e32 v91, 34, v201
	s_nop 0
	v_cndmask_b32_e32 v62, v205, v62, vcc
	v_cmp_le_u32_e32 vcc, v91, v204
	v_add_u32_e32 v91, -2, v201
	s_nop 0
	v_cndmask_b32_e32 v79, v205, v79, vcc
	v_cmp_le_u32_e32 vcc, v91, v204
	v_subrev_u32_e32 v91, 33, v201
	s_nop 0
	v_cndmask_b32_e32 v63, v205, v63, vcc
	v_cmp_le_u32_e32 vcc, v91, v204
	v_add_u32_e32 v91, -1, v201
	s_nop 0
	v_cndmask_b32_e32 v80, v205, v80, vcc
	v_cmp_le_u32_e32 vcc, v91, v204
	v_subrev_u32_e32 v91, 32, v201
	s_nop 0
	v_cndmask_b32_e32 v64, v205, v64, vcc
	v_cmp_le_u32_e32 vcc, v91, v204
	s_nop 1
	v_cndmask_b32_e32 v81, v205, v81, vcc
	v_cmp_le_u32_e32 vcc, v201, v204
	s_nop 1
	v_cndmask_b32_e32 v65, v205, v65, vcc

.LBB1_74:
	v_add_u32_e32 v100, s44, v209
	ds_read_b64_tr_b16 v[178:179], v100 offset:24576
	ds_read_b64_tr_b16 v[180:181], v100 offset:25088
	v_add_f32_e32 v82, v66, v67
	v_add_f32_e32 v82, v68, v82
	v_add_f32_e32 v82, v69, v82
	v_add_f32_e32 v82, v70, v82
	v_add_f32_e32 v98, v71, v82
	s_waitcnt lgkmcnt(9)
	v_mfma_f32_32x32x16_f16 v[82:97], v[174:177], v[142:145], v[34:49]
	v_cvt_pk_f16_f32 v134, v66, v67
	v_cvt_pk_f16_f32 v135, v68, v69
	ds_read_b64_tr_b16 v[174:175], v100 offset:28672
	ds_read_b64_tr_b16 v[176:177], v100 offset:29184
	s_waitcnt lgkmcnt(10)
	v_mfma_f32_32x32x16_f16 v[34:49], v[170:173], v[142:145], v[34:49]
	v_add_f32_e32 v66, v72, v98
	v_add_f32_e32 v66, v73, v66
	v_add_f32_e32 v66, v74, v66
	v_add_f32_e32 v66, v75, v66
	v_cvt_pk_f16_f32 v136, v70, v71
	v_cvt_pk_f16_f32 v137, v72, v73
	ds_read_b64_tr_b16 v[170:171], v100 offset:25600
	ds_read_b64_tr_b16 v[172:173], v100 offset:26112
	s_waitcnt lgkmcnt(11)
	v_mfma_f32_32x32x16_f16 v[82:97], v[166:169], v[138:141], v[82:97]
	v_add_f32_e32 v66, v76, v66
	v_add_f32_e32 v66, v77, v66
	v_add_f32_e32 v66, v78, v66
	v_add_f32_e32 v66, v79, v66
	v_cvt_pk_f16_f32 v126, v74, v75
	v_cvt_pk_f16_f32 v127, v76, v77
	ds_read_b64_tr_b16 v[142:143], v100 offset:29696
	ds_read_b64_tr_b16 v[144:145], v100 offset:30208
	s_waitcnt lgkmcnt(12)
	v_mfma_f32_32x32x16_f16 v[34:49], v[162:165], v[138:141], v[34:49]
	v_add_f32_e32 v66, v80, v66
	v_add_f32_e32 v66, v81, v66
	v_add_f32_e32 v66, v50, v66
	v_add_f32_e32 v66, v51, v66
	v_cvt_pk_f16_f32 v128, v78, v79
	v_cvt_pk_f16_f32 v129, v80, v81
	ds_read_b64_tr_b16 v[110:111], v100 offset:26624
	ds_read_b64_tr_b16 v[112:113], v100 offset:27136
	s_waitcnt lgkmcnt(13)
	v_mfma_f32_32x32x16_f16 v[82:97], v[158:161], v[130:133], v[82:97]
	v_add_f32_e32 v66, v52, v66
	v_add_f32_e32 v66, v53, v66
	v_add_f32_e32 v66, v54, v66
	v_add_f32_e32 v66, v55, v66
	v_cvt_pk_f16_f32 v118, v50, v51
	v_cvt_pk_f16_f32 v119, v52, v53
	ds_read_b64_tr_b16 v[106:107], v100 offset:30720
	ds_read_b64_tr_b16 v[108:109], v100 offset:31232
	s_waitcnt lgkmcnt(14)
	v_mfma_f32_32x32x16_f16 v[34:49], v[154:157], v[130:133], v[34:49]
	v_add_f32_e32 v50, v56, v66
	v_add_f32_e32 v50, v57, v50
	v_add_f32_e32 v50, v58, v50
	v_add_f32_e32 v50, v59, v50
	v_cvt_pk_f16_f32 v120, v54, v55
	v_cvt_pk_f16_f32 v121, v56, v57
	ds_read_b64_tr_b16 v[102:103], v100 offset:27648
	ds_read_b64_tr_b16 v[104:105], v100 offset:28160
	s_waitcnt lgkmcnt(14)
	v_mfma_f32_32x32x16_f16 v[82:97], v[150:153], v[122:125], v[82:97]
	v_add_f32_e32 v50, v60, v50
	v_add_f32_e32 v50, v61, v50
	v_add_f32_e32 v50, v62, v50
	v_add_f32_e32 v50, v63, v50
	v_cvt_pk_f16_f32 v114, v58, v59
	v_cvt_pk_f16_f32 v115, v60, v61
	ds_read_b64_tr_b16 v[98:99], v100 offset:31744
	ds_read_b64_tr_b16 v[100:101], v100 offset:32256
	v_mfma_f32_32x32x16_f16 v[34:49], v[146:149], v[122:125], v[34:49]
	v_add_f32_e32 v50, v64, v50
	v_add_f32_e32 v50, v65, v50
	v_add_f32_e32 v66, 0, v50
	v_cvt_pk_f16_f32 v116, v62, v63
	v_cvt_pk_f16_f32 v117, v64, v65
	s_cmp_lt_u32 s50, 3
	s_cbranch_scc1 .Lmfill_0f
	v_or_b32_e32 v214, 0xe0, v210
	v_or_b32_e32 v213, 0xc0, v210
	v_mov_b32_e32 v67, 0xff800000
	v_cmp_le_u32_e32 vcc, v214, v204
	v_or_b32_e32 v215, 0xe1, v210
	v_or_b32_e32 v216, 0xc2, v210
	s_nop 0
	v_cndmask_b32_e32 v34, v67, v34, vcc
	v_cmp_lt_u32_e32 vcc, v213, v204
	v_or_b32_e32 v217, 0xe2, v210
	v_or_b32_e32 v218, 0xc3, v210
	v_cndmask_b32_e32 v51, v67, v83, vcc
	v_cmp_le_u32_e32 vcc, v213, v204
	v_or_b32_e32 v219, 0xe3, v210
	v_or_b32_e32 v220, 0xc8, v210
	v_cndmask_b32_e32 v50, v67, v82, vcc
	v_cmp_le_u32_e32 vcc, v215, v204
	v_or_b32_e32 v221, 0xe8, v210
	v_or_b32_e32 v222, 0xc9, v210
	v_cndmask_b32_e32 v35, v67, v35, vcc
	v_cmp_le_u32_e32 vcc, v216, v204
	v_or_b32_e32 v223, 0xe9, v210
	v_or_b32_e32 v224, 0xca, v210
	v_cndmask_b32_e32 v52, v67, v84, vcc
	v_cmp_le_u32_e32 vcc, v217, v204
	v_or_b32_e32 v225, 0xea, v210
	v_or_b32_e32 v226, 0xcb, v210
	v_cndmask_b32_e32 v36, v67, v36, vcc
	v_cmp_le_u32_e32 vcc, v218, v204
	v_or_b32_e32 v227, 0xeb, v210
	v_or_b32_e32 v228, 0xd0, v210
	v_cndmask_b32_e32 v53, v67, v85, vcc
	v_cmp_le_u32_e32 vcc, v219, v204
	v_or_b32_e32 v229, 0xf0, v210
	v_or_b32_e32 v230, 0xd1, v210
	v_cndmask_b32_e32 v37, v67, v37, vcc
	v_cmp_le_u32_e32 vcc, v220, v204
	v_or_b32_e32 v231, 0xf1, v210
	v_or_b32_e32 v232, 0xd2, v210
	v_cndmask_b32_e32 v54, v67, v86, vcc
	v_cmp_le_u32_e32 vcc, v221, v204
	v_or_b32_e32 v233, 0xf2, v210
	v_or_b32_e32 v234, 0xd3, v210
	v_cndmask_b32_e32 v38, v67, v38, vcc
	v_cmp_le_u32_e32 vcc, v222, v204
	v_or_b32_e32 v235, 0xf3, v210
	v_or_b32_e32 v236, 0xd8, v210
	v_cndmask_b32_e32 v55, v67, v87, vcc
	v_cmp_le_u32_e32 vcc, v223, v204
	v_or_b32_e32 v237, 0xf8, v210
	v_or_b32_e32 v238, 0xd9, v210
	v_cndmask_b32_e32 v39, v67, v39, vcc
	v_cmp_le_u32_e32 vcc, v224, v204
	v_or_b32_e32 v239, 0xf9, v210
	v_or_b32_e32 v240, 0xda, v210
	v_cndmask_b32_e32 v56, v67, v88, vcc
	v_cmp_le_u32_e32 vcc, v225, v204
	v_or_b32_e32 v241, 0xfa, v210
	v_or_b32_e32 v242, 0xdb, v210
	v_cndmask_b32_e32 v40, v67, v40, vcc
	v_cmp_le_u32_e32 vcc, v226, v204
	v_or_b32_e32 v243, 0xfb, v210
	v_max_f32_e32 v68, v50, v50
	v_cndmask_b32_e32 v57, v67, v89, vcc
	v_cmp_le_u32_e32 vcc, v227, v204
	v_add_f32_e32 v82, v203, v66
	s_mov_b32 s2, 0x41000000
	v_cndmask_b32_e32 v41, v67, v41, vcc
	v_cmp_le_u32_e32 vcc, v228, v204
	s_nop 1
	v_cndmask_b32_e32 v58, v67, v90, vcc
	v_cmp_le_u32_e32 vcc, v229, v204
	s_nop 1
	v_cndmask_b32_e32 v42, v67, v42, vcc
	v_cmp_le_u32_e32 vcc, v230, v204
	s_nop 1
	v_cndmask_b32_e32 v59, v67, v91, vcc
	v_cmp_le_u32_e32 vcc, v231, v204
	s_nop 1
	v_cndmask_b32_e32 v43, v67, v43, vcc
	v_cmp_le_u32_e32 vcc, v232, v204
	s_nop 1
	v_cndmask_b32_e32 v60, v67, v92, vcc
	v_cmp_le_u32_e32 vcc, v233, v204
	s_nop 1
	v_cndmask_b32_e32 v44, v67, v44, vcc
	v_cmp_le_u32_e32 vcc, v234, v204
	s_nop 1
	v_cndmask_b32_e32 v61, v67, v93, vcc
	v_cmp_le_u32_e32 vcc, v235, v204
	s_nop 1
	v_cndmask_b32_e32 v45, v67, v45, vcc
	v_cmp_le_u32_e32 vcc, v236, v204
	s_nop 1
	v_cndmask_b32_e32 v62, v67, v94, vcc
	v_cmp_le_u32_e32 vcc, v237, v204
	s_nop 1
	v_cndmask_b32_e32 v46, v67, v46, vcc
	v_cmp_le_u32_e32 vcc, v238, v204
	s_nop 1
	v_cndmask_b32_e32 v63, v67, v95, vcc
	v_cmp_le_u32_e32 vcc, v239, v204
	s_nop 1
	v_cndmask_b32_e32 v47, v67, v47, vcc
	v_cmp_le_u32_e32 vcc, v240, v204
	s_nop 1
	v_cndmask_b32_e32 v64, v67, v96, vcc
	v_cmp_le_u32_e32 vcc, v241, v204
	s_nop 1
	v_cndmask_b32_e32 v48, v67, v48, vcc
	v_cmp_le_u32_e32 vcc, v242, v204
	s_nop 1
	v_cndmask_b32_e32 v65, v67, v97, vcc
	v_cmp_le_u32_e32 vcc, v243, v204
	s_nop 1
	v_cndmask_b32_e32 v49, v67, v49, vcc
.Lmend_0f:
	v_max_f32_e32 v67, v51, v51
	v_max_f32_e32 v67, v68, v67
	v_max3_f32 v68, v52, v53, v35
	v_max3_f32 v67, v67, v34, v36
	v_max3_f32 v67, v67, v37, v54
	v_max3_f32 v68, v68, v56, v57
	v_max3_f32 v67, v67, v55, v38
	v_max3_f32 v68, v68, v40, v41
	v_max3_f32 v67, v67, v39, v58
	v_max3_f32 v68, v68, v60, v61
	v_max3_f32 v67, v67, v59, v42
	v_max3_f32 v68, v68, v44, v45
	v_max3_f32 v67, v67, v43, v62
	v_max3_f32 v68, v68, v64, v65
	v_max3_f32 v67, v67, v63, v46
	v_max3_f32 v68, v68, v48, v49
	v_max3_f32 v66, v67, v47, v68
	v_mov_b32_e32 v67, v66
	s_nop 1
	v_permlane32_swap_b32_e32 v66, v67
	v_max_f32_e32 v67, v67, v67
	v_max_f32_e32 v66, v66, v66
	v_max_f32_e32 v66, v66, v67
	v_cmp_lt_f32_e32 vcc, s2, v66
	s_cmp_lg_u64 vcc, 0
	s_cselect_b64 s[2:3], -1, 0
	s_cbranch_vccnz .LBB1_160

.LBB1_80:
	v_add_f32_e32 v50, v50, v51
	v_add_f32_e32 v50, v52, v50
	v_add_f32_e32 v50, v53, v50
	v_add_f32_e32 v50, v54, v50
	v_add_f32_e32 v50, v55, v50
	v_add_f32_e32 v50, v56, v50
	v_add_f32_e32 v50, v57, v50
	v_add_f32_e32 v50, v58, v50
	v_add_f32_e32 v50, v59, v50
	v_add_f32_e32 v50, v60, v50
	v_add_f32_e32 v50, v61, v50
	v_add_f32_e32 v50, v62, v50
	v_add_f32_e32 v50, v63, v50
	v_add_f32_e32 v50, v64, v50
	v_add_f32_e32 v50, v65, v50
	v_add_f32_e32 v34, v34, v50
	v_add_f32_e32 v34, v35, v34
	v_add_f32_e32 v34, v36, v34
	v_add_f32_e32 v34, v37, v34
	v_add_f32_e32 v34, v38, v34
	v_add_f32_e32 v34, v39, v34
	v_add_f32_e32 v34, v40, v34
	v_add_f32_e32 v34, v41, v34
	v_add_f32_e32 v34, v42, v34
	v_add_f32_e32 v34, v43, v34
	v_add_f32_e32 v34, v44, v34
	v_add_f32_e32 v34, v45, v34
	v_add_f32_e32 v34, v46, v34
	v_add_f32_e32 v34, v47, v34
	v_add_f32_e32 v34, v48, v34
	v_add_f32_e32 v34, v49, v34
	v_add_f32_e32 v34, v82, v34
	v_mov_b32_e32 v35, v34
	s_nop 1
	v_permlane32_swap_b32_e32 v34, v35
	s_and_saveexec_b64 s[2:3], s[0:1]
	v_add_f32_e32 v34, v34, v35
	ds_write_b32 v198, v34 offset:49280
	s_or_b64 exec, exec, s[2:3]
	s_waitcnt lgkmcnt(0)
	ds_read_b128 v[34:37], v66 offset:49280
	ds_read_b128 v[38:41], v66 offset:49312
	s_mul_i32 s3, s35, 0xe80
	s_mul_hi_u32 s2, s35, 0xe80
	s_add_u32 s3, s10, s3
	s_waitcnt lgkmcnt(1)
	v_rcp_f32_e32 v42, v34
	v_rcp_f32_e32 v43, v35
	s_addc_u32 s4, s11, s2
	s_lshl_b32 s5, s34, 12
	v_lshlrev_b32_e32 v50, 1, v208
	v_lshlrev_b32_e32 v244, 9, v196
	v_rcp_f32_e32 v44, v36
	v_or3_b32 v50, s5, v50, v244
	v_fma_mixlo_f16 v2, v2, v42, 0
	ds_write_b16 v50, v2 offset:51200
	v_fma_mixlo_f16 v2, v18, v42, 0
	v_rcp_f32_e32 v45, v37
	ds_write_b16 v50, v2 offset:51264
	v_fma_mixlo_f16 v2, v3, v43, 0
	ds_write_b16 v50, v2 offset:51328
	v_fma_mixlo_f16 v2, v19, v43, 0
	s_waitcnt lgkmcnt(3)
	v_rcp_f32_e32 v46, v38
	ds_write_b16 v50, v2 offset:51392
	v_fma_mixlo_f16 v2, v4, v44, 0
	ds_write_b16 v50, v2 offset:51456
	v_fma_mixlo_f16 v2, v20, v44, 0
	v_rcp_f32_e32 v47, v39
	ds_write_b16 v50, v2 offset:51520
	v_fma_mixlo_f16 v2, v5, v45, 0
	ds_read_b128 v[34:37], v66 offset:49344
	ds_write_b16 v50, v2 offset:51584
	v_fma_mixlo_f16 v2, v21, v45, 0
	v_rcp_f32_e32 v48, v40
	ds_write_b16 v50, v2 offset:51648
	v_fma_mixlo_f16 v2, v6, v46, 0
	ds_write_b16 v50, v2 offset:52224
	v_fma_mixlo_f16 v2, v22, v46, 0
	v_rcp_f32_e32 v49, v41
	ds_write_b16 v50, v2 offset:52288
	v_fma_mixlo_f16 v2, v7, v47, 0
	ds_write_b16 v50, v2 offset:52352
	v_fma_mixlo_f16 v2, v23, v47, 0
	ds_read_b128 v[38:41], v66 offset:49376
	s_waitcnt lgkmcnt(6)
	v_rcp_f32_e32 v34, v34
	ds_write_b16 v50, v2 offset:52416
	v_fma_mixlo_f16 v2, v8, v48, 0
	ds_write_b16 v50, v2 offset:52480
	v_fma_mixlo_f16 v2, v24, v48, 0
	v_rcp_f32_e32 v35, v35
	ds_write_b16 v50, v2 offset:52544
	v_fma_mixlo_f16 v2, v9, v49, 0
	ds_write_b16 v50, v2 offset:52608
	v_fma_mixlo_f16 v2, v25, v49, 0
	v_rcp_f32_e32 v36, v36
	ds_write_b16 v50, v2 offset:52672
	v_fma_mixlo_f16 v2, v10, v34, 0
	ds_write_b16 v50, v2 offset:53248
	v_fma_mixlo_f16 v2, v26, v34, 0
	v_rcp_f32_e32 v37, v37
	ds_write_b16 v50, v2 offset:53312
	v_fma_mixlo_f16 v2, v11, v35, 0
	ds_write_b16 v50, v2 offset:53376
	v_fma_mixlo_f16 v2, v27, v35, 0
	s_waitcnt lgkmcnt(8)
	v_rcp_f32_e32 v38, v38
	ds_write_b16 v50, v2 offset:53440
	v_fma_mixlo_f16 v2, v12, v36, 0
	ds_write_b16 v50, v2 offset:53504
	v_fma_mixlo_f16 v2, v28, v36, 0
	v_rcp_f32_e32 v39, v39
	ds_write_b16 v50, v2 offset:53568
	v_fma_mixlo_f16 v2, v13, v37, 0
	ds_write_b16 v50, v2 offset:53632
	v_fma_mixlo_f16 v2, v29, v37, 0
	v_rcp_f32_e32 v40, v40
	ds_write_b16 v50, v2 offset:53696
	v_fma_mixlo_f16 v2, v14, v38, 0
	ds_write_b16 v50, v2 offset:54272
	v_fma_mixlo_f16 v2, v30, v38, 0
	v_rcp_f32_e32 v41, v41
	ds_write_b16 v50, v2 offset:54336
	v_fma_mixlo_f16 v2, v15, v39, 0
	ds_write_b16 v50, v2 offset:54400
	v_fma_mixlo_f16 v2, v31, v39, 0
	ds_write_b16 v50, v2 offset:54464
	v_fma_mixlo_f16 v2, v16, v40, 0
	ds_write_b16 v50, v2 offset:54528
	v_fma_mixlo_f16 v2, v32, v40, 0
	ds_write_b16 v50, v2 offset:54592
	v_fma_mixlo_f16 v2, v17, v41, 0
	ds_write_b16 v50, v2 offset:54656
	v_fma_mixlo_f16 v2, v33, v41, 0
	ds_write_b16 v50, v2 offset:54720
	v_and_b32_e32 v2, 56, v197
	v_lshrrev_b32_e32 v8, 3, v195
	v_lshlrev_b32_e32 v204, 1, v2
	s_add_u32 s2, s3, s14
	v_or_b32_e32 v14, s5, v204
	v_lshlrev_b32_e32 v245, 7, v8
	s_addc_u32 s3, s4, s15
	s_waitcnt lgkmcnt(0)
	v_mov_b32_e32 v205, 0
	v_or_b32_e32 v2, v14, v245
	v_mul_u32_u24_e32 v8, 0x740, v8
	v_lshl_add_u64 v[6:7], s[2:3], 0, v[204:205]
	ds_read_b128 v[2:5], v2 offset:51200
	v_lshlrev_b32_e32 v206, 1, v8
	v_mov_b32_e32 v207, v205
	v_or_b32_e32 v246, 0x400, v245
	v_lshl_add_u64 v[10:11], v[6:7], 0, v[206:207]
	v_or_b32_e32 v6, v14, v246
	ds_read_b128 v[6:9], v6 offset:51200
	s_movk_i32 s2, 0x7000
	s_waitcnt lgkmcnt(1)
	global_store_dwordx4 v[10:11], v[2:5], off sc0 sc1
	v_or_b32_e32 v247, 0x800, v245
	v_or_b32_e32 v248, 0xc00, v245
	v_add_co_u32_e32 v2, vcc, s2, v10
	s_mov_b32 s2, 0xe000
	s_nop 0
	v_addc_co_u32_e32 v3, vcc, 0, v11, vcc
	s_waitcnt lgkmcnt(0)
	global_store_dwordx4 v[2:3], v[6:9], off offset:1024 sc0 sc1
	v_or_b32_e32 v2, v14, v247
	ds_read_b128 v[2:5], v2 offset:51200
	v_or_b32_e32 v6, v14, v248
	ds_read_b128 v[6:9], v6 offset:51200
	v_add_co_u32_e32 v12, vcc, s2, v10
	s_nop 1
	v_addc_co_u32_e32 v13, vcc, 0, v11, vcc
	s_waitcnt lgkmcnt(1)
	global_store_dwordx4 v[12:13], v[2:5], off offset:2048 sc0 sc1
	s_nop 1
	v_add_co_u32_e32 v2, vcc, 0x15000, v10
	s_nop 1
	v_addc_co_u32_e32 v3, vcc, 0, v11, vcc
	s_waitcnt lgkmcnt(0)
	global_store_dwordx4 v[2:3], v[6:9], off offset:3072 sc0 sc1
	s_waitcnt lgkmcnt(0)
	s_barrier
	s_andn2_b64 vcc, exec, s[12:13]
	s_cbranch_vccnz .LBB1_109
	s_mov_b32 s2, 0x14800
	v_mov_b32_e32 v2, v205
	v_mov_b32_e32 v3, v205
	v_mov_b32_e32 v4, v205
	v_mov_b32_e32 v5, v205
	v_mov_b32_e32 v6, v205
	v_mov_b32_e32 v7, v205
	v_mov_b32_e32 v8, v205
	v_mov_b32_e32 v9, v205
	v_mov_b32_e32 v10, v205
	v_mov_b32_e32 v11, v205
	v_mov_b32_e32 v12, v205
	v_mov_b32_e32 v13, v205
	v_mov_b32_e32 v14, v205
	v_mov_b32_e32 v15, v205
	v_mov_b32_e32 v16, v205
	v_mov_b32_e32 v17, v205
	v_add3_u32 v250, v194, v193, s2
	s_waitcnt vmcnt(4) lgkmcnt(0)
	s_barrier
	ds_read_b128 v[34:37], v250
	s_waitcnt lgkmcnt(0)
	v_mfma_f32_32x32x16_f16 v[18:33], v[34:37], v[140:143], v[2:17]
	ds_read_b128 v[34:37], v250 offset:512
	v_readfirstlane_b32 s4, v0
	s_lshr_b32 s18, s4, 6
	s_lshl_b32 s19, s18, 5
	s_cmp_lg_u32 s30, 0
	s_cselect_b64 s[2:3], -1, 0
	v_or_b32_e32 v207, s19, v208
	s_waitcnt lgkmcnt(0)
	v_mfma_f32_32x32x16_f16 v[2:17], v[34:37], v[140:143], v[2:17]
	ds_read_b128 v[34:37], v250 offset:2048
	s_and_b64 vcc, exec, s[2:3]
	s_waitcnt lgkmcnt(0)
	v_mfma_f32_32x32x16_f16 v[18:33], v[34:37], v[136:139], v[18:33]
	ds_read_b128 v[34:37], v250 offset:2560
	s_waitcnt lgkmcnt(0)
	v_mfma_f32_32x32x16_f16 v[2:17], v[34:37], v[136:139], v[2:17]
	ds_read_b128 v[34:37], v250 offset:4096
	s_waitcnt lgkmcnt(0)
	v_mfma_f32_32x32x16_f16 v[18:33], v[34:37], v[132:135], v[18:33]
	ds_read_b128 v[34:37], v250 offset:4608
	s_waitcnt lgkmcnt(0)
	v_mfma_f32_32x32x16_f16 v[2:17], v[34:37], v[132:135], v[2:17]
	ds_read_b128 v[34:37], v250 offset:6144
	s_waitcnt lgkmcnt(0)
	v_mfma_f32_32x32x16_f16 v[18:33], v[34:37], v[128:131], v[18:33]
	ds_read_b128 v[34:37], v250 offset:6656
	s_waitcnt lgkmcnt(0)
	v_mfma_f32_32x32x16_f16 v[2:17], v[34:37], v[128:131], v[2:17]
	s_nop 15
	s_nop 7
	s_cbranch_vccnz .LBB1_85
	s_cmp_lg_u32 s50, 0
	s_cbranch_scc1 .LBB1_85
	v_or_b32_e32 v0, 32, v210
	v_mov_b32_e32 v34, 0xff800000
	v_cmp_le_u32_e32 vcc, v0, v207
	v_or_b32_e32 v0, 33, v210
	s_nop 6
	v_cndmask_b32_e32 v2, v34, v2, vcc
	v_cmp_lt_u32_e32 vcc, v210, v207
	s_nop 1
	v_cndmask_b32_e32 v19, v34, v19, vcc
	v_cmp_le_u32_e32 vcc, v210, v207
	s_nop 1
	v_cndmask_b32_e32 v18, v34, v18, vcc
	v_cmp_le_u32_e32 vcc, v0, v207
	v_or_b32_e32 v0, 2, v210
	s_nop 0
	v_cndmask_b32_e32 v3, v34, v3, vcc
	v_cmp_le_u32_e32 vcc, v0, v207
	v_or_b32_e32 v0, 34, v210
	s_nop 0
	v_cndmask_b32_e32 v20, v34, v20, vcc
	v_cmp_le_u32_e32 vcc, v0, v207
	v_or_b32_e32 v0, 3, v210
	s_nop 0
	v_cndmask_b32_e32 v4, v34, v4, vcc
	v_cmp_le_u32_e32 vcc, v0, v207
	v_or_b32_e32 v0, 35, v210
	s_nop 0
	v_cndmask_b32_e32 v21, v34, v21, vcc
	v_cmp_le_u32_e32 vcc, v0, v207
	v_or_b32_e32 v0, 8, v210
	s_nop 0
	v_cndmask_b32_e32 v5, v34, v5, vcc
	v_cmp_le_u32_e32 vcc, v0, v207
	v_or_b32_e32 v0, 40, v210
	s_nop 0
	v_cndmask_b32_e32 v22, v34, v22, vcc
	v_cmp_le_u32_e32 vcc, v0, v207
	v_or_b32_e32 v0, 9, v210
	s_nop 0
	v_cndmask_b32_e32 v6, v34, v6, vcc
	v_cmp_le_u32_e32 vcc, v0, v207
	v_or_b32_e32 v0, 41, v210
	s_nop 0
	v_cndmask_b32_e32 v23, v34, v23, vcc
	v_cmp_le_u32_e32 vcc, v0, v207
	v_or_b32_e32 v0, 10, v210
	s_nop 0
	v_cndmask_b32_e32 v7, v34, v7, vcc
	v_cmp_le_u32_e32 vcc, v0, v207
	v_or_b32_e32 v0, 42, v210
	s_nop 0
	v_cndmask_b32_e32 v24, v34, v24, vcc
	v_cmp_le_u32_e32 vcc, v0, v207
	v_or_b32_e32 v0, 11, v210
	s_nop 0
	v_cndmask_b32_e32 v8, v34, v8, vcc
	v_cmp_le_u32_e32 vcc, v0, v207
	v_or_b32_e32 v0, 43, v210
	s_nop 0
	v_cndmask_b32_e32 v25, v34, v25, vcc
	v_cmp_le_u32_e32 vcc, v0, v207
	v_or_b32_e32 v0, 16, v210
	s_nop 0
	v_cndmask_b32_e32 v9, v34, v9, vcc
	v_cmp_le_u32_e32 vcc, v0, v207
	v_or_b32_e32 v0, 48, v210
	s_nop 0
	v_cndmask_b32_e32 v26, v34, v26, vcc
	v_cmp_le_u32_e32 vcc, v0, v207
	v_or_b32_e32 v0, 17, v210
	s_nop 0
	v_cndmask_b32_e32 v10, v34, v10, vcc
	v_cmp_le_u32_e32 vcc, v0, v207
	v_or_b32_e32 v0, 49, v210
	s_nop 0
	v_cndmask_b32_e32 v27, v34, v27, vcc
	v_cmp_le_u32_e32 vcc, v0, v207
	v_or_b32_e32 v0, 18, v210
	s_nop 0
	v_cndmask_b32_e32 v11, v34, v11, vcc
	v_cmp_le_u32_e32 vcc, v0, v207
	v_or_b32_e32 v0, 50, v210
	s_nop 0
	v_cndmask_b32_e32 v28, v34, v28, vcc
	v_cmp_le_u32_e32 vcc, v0, v207
	v_or_b32_e32 v0, 19, v210
	s_nop 0
	v_cndmask_b32_e32 v12, v34, v12, vcc
	v_cmp_le_u32_e32 vcc, v0, v207
	v_or_b32_e32 v0, 51, v210
	s_nop 0
	v_cndmask_b32_e32 v29, v34, v29, vcc
	v_cmp_le_u32_e32 vcc, v0, v207
	v_or_b32_e32 v0, 24, v210
	s_nop 0
	v_cndmask_b32_e32 v13, v34, v13, vcc
	v_cmp_le_u32_e32 vcc, v0, v207
	v_or_b32_e32 v0, 56, v210
	s_nop 0
	v_cndmask_b32_e32 v30, v34, v30, vcc
	v_cmp_le_u32_e32 vcc, v0, v207
	v_or_b32_e32 v0, 25, v210
	s_nop 0
	v_cndmask_b32_e32 v14, v34, v14, vcc
	v_cmp_le_u32_e32 vcc, v0, v207
	v_or_b32_e32 v0, 57, v210
	s_nop 0
	v_cndmask_b32_e32 v31, v34, v31, vcc
	v_cmp_le_u32_e32 vcc, v0, v207
	v_or_b32_e32 v0, 26, v210
	s_nop 0
	v_cndmask_b32_e32 v15, v34, v15, vcc
	v_cmp_le_u32_e32 vcc, v0, v207
	v_or_b32_e32 v0, 58, v210
	s_nop 0
	v_cndmask_b32_e32 v32, v34, v32, vcc
	v_cmp_le_u32_e32 vcc, v0, v207
	v_or_b32_e32 v0, 27, v210
	s_nop 0
	v_cndmask_b32_e32 v16, v34, v16, vcc
	v_cmp_le_u32_e32 vcc, v0, v207
	v_or_b32_e32 v0, 59, v210
	s_nop 0
	v_cndmask_b32_e32 v33, v34, v33, vcc
	v_cmp_le_u32_e32 vcc, v0, v207
	s_nop 1
	v_cndmask_b32_e32 v17, v34, v17, vcc

.LBB1_103:
	v_add_u32_e32 v65, s26, v251
	ds_read_b64_tr_b16 v[124:125], v65
	ds_read_b64_tr_b16 v[126:127], v65 offset:512
	s_waitcnt lgkmcnt(9)
	v_mfma_f32_32x32x16_f16 v[96:111], v[188:191], v[140:143], v[32:47]
	v_add_f32_e32 v66, v80, v81
	v_add_f32_e32 v66, v82, v66
	v_add_f32_e32 v66, v83, v66
	v_add_f32_e32 v66, v84, v66
	v_add_f32_e32 v66, v85, v66
	v_cvt_pk_f16_f32 v156, v80, v81
	v_cvt_pk_f16_f32 v157, v82, v83
	ds_read_b64_tr_b16 v[120:121], v65 offset:4096
	ds_read_b64_tr_b16 v[122:123], v65 offset:4608
	s_waitcnt lgkmcnt(10)
	v_mfma_f32_32x32x16_f16 v[32:47], v[184:187], v[140:143], v[32:47]
	v_add_f32_e32 v66, v86, v66
	v_add_f32_e32 v66, v87, v66
	v_add_f32_e32 v66, v88, v66
	v_add_f32_e32 v66, v89, v66
	v_cvt_pk_f16_f32 v158, v84, v85
	v_cvt_pk_f16_f32 v159, v86, v87
	ds_read_b64_tr_b16 v[116:117], v65 offset:1024
	ds_read_b64_tr_b16 v[118:119], v65 offset:1536
	s_waitcnt lgkmcnt(11)
	v_mfma_f32_32x32x16_f16 v[96:111], v[180:183], v[136:139], v[96:111]
	v_add_f32_e32 v66, v90, v66
	v_add_f32_e32 v66, v91, v66
	v_add_f32_e32 v66, v92, v66
	v_add_f32_e32 v66, v93, v66
	v_cvt_pk_f16_f32 v152, v88, v89
	v_cvt_pk_f16_f32 v153, v90, v91
	ds_read_b64_tr_b16 v[112:113], v65 offset:5120
	ds_read_b64_tr_b16 v[114:115], v65 offset:5632
	s_waitcnt lgkmcnt(12)
	v_mfma_f32_32x32x16_f16 v[32:47], v[176:179], v[136:139], v[32:47]
	v_add_f32_e32 v66, v94, v66
	v_add_f32_e32 v66, v95, v66
	v_add_f32_e32 v66, v48, v66
	v_add_f32_e32 v66, v49, v66
	v_cvt_pk_f16_f32 v154, v92, v93
	v_cvt_pk_f16_f32 v155, v94, v95
	ds_read_b64_tr_b16 v[92:93], v65 offset:2048
	ds_read_b64_tr_b16 v[94:95], v65 offset:2560
	s_waitcnt lgkmcnt(13)
	v_mfma_f32_32x32x16_f16 v[96:111], v[172:175], v[132:135], v[96:111]
	v_add_f32_e32 v66, v50, v66
	v_add_f32_e32 v66, v51, v66
	v_add_f32_e32 v66, v52, v66
	v_add_f32_e32 v66, v53, v66
	v_cvt_pk_f16_f32 v148, v48, v49
	v_cvt_pk_f16_f32 v149, v50, v51
	ds_read_b64_tr_b16 v[88:89], v65 offset:6144
	ds_read_b64_tr_b16 v[90:91], v65 offset:6656
	s_waitcnt lgkmcnt(14)
	v_mfma_f32_32x32x16_f16 v[32:47], v[168:171], v[132:135], v[32:47]
	v_add_f32_e32 v48, v54, v66
	v_add_f32_e32 v48, v55, v48
	v_add_f32_e32 v48, v56, v48
	v_add_f32_e32 v48, v57, v48
	v_cvt_pk_f16_f32 v150, v52, v53
	v_cvt_pk_f16_f32 v151, v54, v55
	ds_read_b64_tr_b16 v[84:85], v65 offset:3072
	ds_read_b64_tr_b16 v[86:87], v65 offset:3584
	s_waitcnt lgkmcnt(14)
	v_mfma_f32_32x32x16_f16 v[96:111], v[164:167], v[128:131], v[96:111]
	v_add_f32_e32 v48, v58, v48
	v_add_f32_e32 v48, v59, v48
	v_add_f32_e32 v48, v60, v48
	v_add_f32_e32 v48, v61, v48
	v_cvt_pk_f16_f32 v144, v56, v57
	v_cvt_pk_f16_f32 v145, v58, v59
	ds_read_b64_tr_b16 v[80:81], v65 offset:7168
	ds_read_b64_tr_b16 v[82:83], v65 offset:7680
	v_mfma_f32_32x32x16_f16 v[32:47], v[160:163], v[128:131], v[32:47]
	v_add_f32_e32 v48, v62, v48
	v_add_f32_e32 v48, v63, v48
	v_add_f32_e32 v65, 0, v48
	v_cvt_pk_f16_f32 v146, v60, v61
	v_cvt_pk_f16_f32 v147, v62, v63
	s_cmp_lt_u32 s50, 3
	s_cbranch_scc1 .Lmfill_1f
	v_mov_b32_e32 v66, 0xff800000
	v_cmp_le_u32_e32 vcc, v214, v207
	s_mov_b32 s2, 0x41000000
	s_nop 3
	v_cndmask_b32_e32 v32, v66, v32, vcc
	v_cmp_lt_u32_e32 vcc, v213, v207
	s_nop 1
	v_cndmask_b32_e32 v49, v66, v97, vcc
	v_cmp_le_u32_e32 vcc, v213, v207
	s_nop 1
	v_cndmask_b32_e32 v48, v66, v96, vcc
	v_cmp_le_u32_e32 vcc, v215, v207
	v_max_f32_e32 v67, v48, v48
	v_add_f32_e32 v96, v64, v65
	v_cndmask_b32_e32 v33, v66, v33, vcc
	v_cmp_le_u32_e32 vcc, v216, v207
	s_nop 1
	v_cndmask_b32_e32 v50, v66, v98, vcc
	v_cmp_le_u32_e32 vcc, v217, v207
	s_nop 1
	v_cndmask_b32_e32 v34, v66, v34, vcc
	v_cmp_le_u32_e32 vcc, v218, v207
	s_nop 1
	v_cndmask_b32_e32 v51, v66, v99, vcc
	v_cmp_le_u32_e32 vcc, v219, v207
	s_nop 1
	v_cndmask_b32_e32 v35, v66, v35, vcc
	v_cmp_le_u32_e32 vcc, v220, v207
	s_nop 1
	v_cndmask_b32_e32 v52, v66, v100, vcc
	v_cmp_le_u32_e32 vcc, v221, v207
	s_nop 1
	v_cndmask_b32_e32 v36, v66, v36, vcc
	v_cmp_le_u32_e32 vcc, v222, v207
	s_nop 1
	v_cndmask_b32_e32 v53, v66, v101, vcc
	v_cmp_le_u32_e32 vcc, v223, v207
	s_nop 1
	v_cndmask_b32_e32 v37, v66, v37, vcc
	v_cmp_le_u32_e32 vcc, v224, v207
	s_nop 1
	v_cndmask_b32_e32 v54, v66, v102, vcc
	v_cmp_le_u32_e32 vcc, v225, v207
	s_nop 1
	v_cndmask_b32_e32 v38, v66, v38, vcc
	v_cmp_le_u32_e32 vcc, v226, v207
	s_nop 1
	v_cndmask_b32_e32 v55, v66, v103, vcc
	v_cmp_le_u32_e32 vcc, v227, v207
	s_nop 1
	v_cndmask_b32_e32 v39, v66, v39, vcc
	v_cmp_le_u32_e32 vcc, v228, v207
	s_nop 1
	v_cndmask_b32_e32 v56, v66, v104, vcc
	v_cmp_le_u32_e32 vcc, v229, v207
	s_nop 1
	v_cndmask_b32_e32 v40, v66, v40, vcc
	v_cmp_le_u32_e32 vcc, v230, v207
	s_nop 1
	v_cndmask_b32_e32 v57, v66, v105, vcc
	v_cmp_le_u32_e32 vcc, v231, v207
	s_nop 1
	v_cndmask_b32_e32 v41, v66, v41, vcc
	v_cmp_le_u32_e32 vcc, v232, v207
	s_nop 1
	v_cndmask_b32_e32 v58, v66, v106, vcc
	v_cmp_le_u32_e32 vcc, v233, v207
	s_nop 1
	v_cndmask_b32_e32 v42, v66, v42, vcc
	v_cmp_le_u32_e32 vcc, v234, v207
	s_nop 1
	v_cndmask_b32_e32 v59, v66, v107, vcc
	v_cmp_le_u32_e32 vcc, v235, v207
	s_nop 1
	v_cndmask_b32_e32 v43, v66, v43, vcc
	v_cmp_le_u32_e32 vcc, v236, v207
	s_nop 1
	v_cndmask_b32_e32 v60, v66, v108, vcc
	v_cmp_le_u32_e32 vcc, v237, v207
	s_nop 1
	v_cndmask_b32_e32 v44, v66, v44, vcc
	v_cmp_le_u32_e32 vcc, v238, v207
	s_nop 1
	v_cndmask_b32_e32 v61, v66, v109, vcc
	v_cmp_le_u32_e32 vcc, v239, v207
	s_nop 1
	v_cndmask_b32_e32 v45, v66, v45, vcc
	v_cmp_le_u32_e32 vcc, v240, v207
	s_nop 1
	v_cndmask_b32_e32 v62, v66, v110, vcc
	v_cmp_le_u32_e32 vcc, v241, v207
	s_nop 1
	v_cndmask_b32_e32 v46, v66, v46, vcc
	v_cmp_le_u32_e32 vcc, v242, v207
	s_nop 1
	v_cndmask_b32_e32 v63, v66, v111, vcc
	v_cmp_le_u32_e32 vcc, v243, v207
	s_nop 1
	v_cndmask_b32_e32 v47, v66, v47, vcc
.Lmend_1f:
	v_max_f32_e32 v66, v49, v49
	v_max_f32_e32 v66, v67, v66
	v_max3_f32 v67, v50, v51, v33
	v_max3_f32 v66, v66, v32, v34
	v_max3_f32 v66, v66, v35, v52
	v_max3_f32 v67, v67, v54, v55
	v_max3_f32 v66, v66, v53, v36
	v_max3_f32 v67, v67, v38, v39
	v_max3_f32 v66, v66, v37, v56
	v_max3_f32 v67, v67, v58, v59
	v_max3_f32 v66, v66, v57, v40
	v_max3_f32 v67, v67, v42, v43
	v_max3_f32 v66, v66, v41, v60
	v_max3_f32 v67, v67, v62, v63
	v_max3_f32 v66, v66, v61, v44
	v_max3_f32 v67, v67, v46, v47
	v_max3_f32 v64, v66, v45, v67
	v_mov_b32_e32 v65, v64
	s_nop 1
	v_permlane32_swap_b32_e32 v64, v65
	v_max_f32_e32 v65, v65, v65
	v_max_f32_e32 v64, v64, v64
	v_max_f32_e32 v64, v64, v65
	v_cmp_lt_f32_e32 vcc, s2, v64
	s_cmp_lg_u64 vcc, 0
	s_cselect_b64 s[2:3], -1, 0
	s_cbranch_vccnz .LBB1_163

.LBB1_114:
	s_add_i32 s14, s27, s31
	s_add_i32 s2, s26, s23
	s_add_i32 s3, s14, 2
	s_mov_b32 s51, s3
	s_cmp_lt_i32 s3, s50
	s_mov_b32 s3, m0
	s_mov_b32 m0, s2
	s_nop 0
	global_load_lds_dwordx4 v211, s[4:5]
	s_mov_b32 m0, s3
	s_cbranch_scc1 .LBB1_116
	s_cmp_gt_i32 s51, s50
	s_cbranch_scc1 .Lmfill_1a
	v_add_u32_e32 v58, 0xffffffa5, v65
	v_add_u32_e32 v57, 0xffffff85, v65
	v_cmp_le_i32_e32 vcc, v58, v207
	s_nop 1
	v_cndmask_b32_e32 v96, v252, v96, vcc
	v_cmp_lt_i32_e32 vcc, v57, v207
	s_nop 1
	v_cndmask_b32_e32 v113, v252, v113, vcc
	v_cmp_le_i32_e32 vcc, v57, v207
	v_add_u32_e32 v57, 0xffffffa6, v65
	s_nop 0
	v_cndmask_b32_e32 v112, v252, v112, vcc
	v_cmp_le_i32_e32 vcc, v57, v207
	v_add_u32_e32 v57, 0xffffff87, v65
	s_nop 0
	v_cndmask_b32_e32 v97, v252, v97, vcc
	v_cmp_le_i32_e32 vcc, v57, v207
	v_add_u32_e32 v57, 0xffffffa7, v65
	s_nop 0
	v_cndmask_b32_e32 v114, v252, v114, vcc
	v_cmp_le_i32_e32 vcc, v57, v207
	v_add_u32_e32 v57, 0xffffff88, v65
	s_nop 0
	v_cndmask_b32_e32 v98, v252, v98, vcc
	v_cmp_le_i32_e32 vcc, v57, v207
	v_add_u32_e32 v57, 0xffffffa8, v65
	s_nop 0
	v_cndmask_b32_e32 v115, v252, v115, vcc
	v_cmp_le_i32_e32 vcc, v57, v207
	v_add_u32_e32 v57, 0xffffff8d, v65
	s_nop 0
	v_cndmask_b32_e32 v99, v252, v99, vcc
	v_cmp_le_i32_e32 vcc, v57, v207
	v_add_u32_e32 v57, 0xffffffad, v65
	s_nop 0
	v_cndmask_b32_e32 v116, v252, v116, vcc
	v_cmp_le_i32_e32 vcc, v57, v207
	v_add_u32_e32 v57, 0xffffff8e, v65
	s_nop 0
	v_cndmask_b32_e32 v100, v252, v100, vcc
	v_cmp_le_i32_e32 vcc, v57, v207
	v_add_u32_e32 v57, 0xffffffae, v65
	s_nop 0
	v_cndmask_b32_e32 v117, v252, v117, vcc
	v_cmp_le_i32_e32 vcc, v57, v207
	v_add_u32_e32 v57, 0xffffff8f, v65
	s_nop 0
	v_cndmask_b32_e32 v101, v252, v101, vcc
	v_cmp_le_i32_e32 vcc, v57, v207
	v_add_u32_e32 v57, 0xffffffaf, v65
	s_nop 0
	v_cndmask_b32_e32 v118, v252, v118, vcc
	v_cmp_le_i32_e32 vcc, v57, v207
	v_add_u32_e32 v57, 0xffffff90, v65
	s_nop 0
	v_cndmask_b32_e32 v102, v252, v102, vcc
	v_cmp_le_i32_e32 vcc, v57, v207
	v_add_u32_e32 v57, 0xffffffb0, v65
	s_nop 0
	v_cndmask_b32_e32 v119, v252, v119, vcc
	v_cmp_le_i32_e32 vcc, v57, v207
	v_add_u32_e32 v57, 0xffffff95, v65
	s_nop 0
	v_cndmask_b32_e32 v103, v252, v103, vcc
	v_cmp_le_i32_e32 vcc, v57, v207
	v_add_u32_e32 v57, 0xffffffb5, v65
	s_nop 0
	v_cndmask_b32_e32 v120, v252, v120, vcc
	v_cmp_le_i32_e32 vcc, v57, v207
	v_add_u32_e32 v57, 0xffffff96, v65
	s_nop 0
	v_cndmask_b32_e32 v104, v252, v104, vcc
	v_cmp_le_i32_e32 vcc, v57, v207
	v_add_u32_e32 v57, 0xffffffb6, v65
	s_nop 0
	v_cndmask_b32_e32 v121, v252, v121, vcc
	v_cmp_le_i32_e32 vcc, v57, v207
	v_add_u32_e32 v57, 0xffffff97, v65
	s_nop 0
	v_cndmask_b32_e32 v105, v252, v105, vcc
	v_cmp_le_i32_e32 vcc, v57, v207
	v_add_u32_e32 v57, 0xffffffb7, v65
	s_nop 0
	v_cndmask_b32_e32 v122, v252, v122, vcc
	v_cmp_le_i32_e32 vcc, v57, v207
	v_add_u32_e32 v57, 0xffffff98, v65
	s_nop 0
	v_cndmask_b32_e32 v106, v252, v106, vcc
	v_cmp_le_i32_e32 vcc, v57, v207
	v_add_u32_e32 v57, 0xffffffb8, v65
	s_nop 0
	v_cndmask_b32_e32 v123, v252, v123, vcc
	v_cmp_le_i32_e32 vcc, v57, v207
	v_add_u32_e32 v57, 0xffffff9d, v65
	s_nop 0
	v_cndmask_b32_e32 v107, v252, v107, vcc
	v_cmp_le_i32_e32 vcc, v57, v207
	v_add_u32_e32 v57, 0xffffffbd, v65
	s_nop 0
	v_cndmask_b32_e32 v124, v252, v124, vcc
	v_cmp_le_i32_e32 vcc, v57, v207
	v_add_u32_e32 v57, 0xffffff9e, v65
	s_nop 0
	v_cndmask_b32_e32 v108, v252, v108, vcc
	v_cmp_le_i32_e32 vcc, v57, v207
	v_add_u32_e32 v57, 0xffffffbe, v65
	s_nop 0
	v_cndmask_b32_e32 v125, v252, v125, vcc
	v_cmp_le_i32_e32 vcc, v57, v207
	v_add_u32_e32 v57, 0xffffff9f, v65
	s_nop 0
	v_cndmask_b32_e32 v109, v252, v109, vcc
	v_cmp_le_i32_e32 vcc, v57, v207
	v_add_u32_e32 v57, 0xffffffbf, v65
	s_nop 0
	v_cndmask_b32_e32 v126, v252, v126, vcc
	v_cmp_le_i32_e32 vcc, v57, v207
	v_add_u32_e32 v57, 0xffffffa0, v65
	s_nop 0
	v_cndmask_b32_e32 v110, v252, v110, vcc
	v_cmp_le_i32_e32 vcc, v57, v207
	v_subrev_u32_e32 v57, 64, v65
	s_nop 0
	v_cndmask_b32_e32 v127, v252, v127, vcc
	v_cmp_le_i32_e32 vcc, v57, v207
	s_nop 1
	v_cndmask_b32_e32 v111, v252, v111, vcc

.LBB1_125:
	s_add_i32 s14, s14, 3
	s_cmp_lt_i32 s14, s50
	s_cbranch_scc1 .LBB1_127
	s_cmp_gt_i32 s14, s50
	s_cbranch_scc1 .Lmfill_1b
	v_subrev_u32_e32 v97, 27, v65
	v_subrev_u32_e32 v96, 59, v65
	v_cmp_le_u32_e32 vcc, v97, v207
	s_nop 1
	v_cndmask_b32_e32 v48, v252, v48, vcc
	v_cmp_lt_u32_e32 vcc, v96, v207
	s_nop 1
	v_cndmask_b32_e32 v81, v252, v81, vcc
	v_cmp_le_u32_e32 vcc, v96, v207
	v_subrev_u32_e32 v96, 26, v65
	s_nop 0
	v_cndmask_b32_e32 v80, v252, v80, vcc
	v_cmp_le_u32_e32 vcc, v96, v207
	v_subrev_u32_e32 v96, 57, v65
	s_nop 0
	v_cndmask_b32_e32 v49, v252, v49, vcc
	v_cmp_le_u32_e32 vcc, v96, v207
	v_subrev_u32_e32 v96, 25, v65
	s_nop 0
	v_cndmask_b32_e32 v82, v252, v82, vcc
	v_cmp_le_u32_e32 vcc, v96, v207
	v_subrev_u32_e32 v96, 56, v65
	s_nop 0
	v_cndmask_b32_e32 v50, v252, v50, vcc
	v_cmp_le_u32_e32 vcc, v96, v207
	v_subrev_u32_e32 v96, 24, v65
	s_nop 0
	v_cndmask_b32_e32 v83, v252, v83, vcc
	v_cmp_le_u32_e32 vcc, v96, v207
	v_subrev_u32_e32 v96, 51, v65
	s_nop 0
	v_cndmask_b32_e32 v51, v252, v51, vcc
	v_cmp_le_u32_e32 vcc, v96, v207
	v_subrev_u32_e32 v96, 19, v65
	s_nop 0
	v_cndmask_b32_e32 v84, v252, v84, vcc
	v_cmp_le_u32_e32 vcc, v96, v207
	v_subrev_u32_e32 v96, 50, v65
	s_nop 0
	v_cndmask_b32_e32 v52, v252, v52, vcc
	v_cmp_le_u32_e32 vcc, v96, v207
	v_subrev_u32_e32 v96, 18, v65
	s_nop 0
	v_cndmask_b32_e32 v85, v252, v85, vcc
	v_cmp_le_u32_e32 vcc, v96, v207
	v_subrev_u32_e32 v96, 49, v65
	s_nop 0
	v_cndmask_b32_e32 v53, v252, v53, vcc
	v_cmp_le_u32_e32 vcc, v96, v207
	v_subrev_u32_e32 v96, 17, v65
	s_nop 0
	v_cndmask_b32_e32 v86, v252, v86, vcc
	v_cmp_le_u32_e32 vcc, v96, v207
	v_subrev_u32_e32 v96, 48, v65
	s_nop 0
	v_cndmask_b32_e32 v54, v252, v54, vcc
	v_cmp_le_u32_e32 vcc, v96, v207
	v_add_u32_e32 v96, -16, v65
	s_nop 0
	v_cndmask_b32_e32 v87, v252, v87, vcc
	v_cmp_le_u32_e32 vcc, v96, v207
	v_subrev_u32_e32 v96, 43, v65
	s_nop 0
	v_cndmask_b32_e32 v55, v252, v55, vcc
	v_cmp_le_u32_e32 vcc, v96, v207
	v_add_u32_e32 v96, -11, v65
	s_nop 0
	v_cndmask_b32_e32 v88, v252, v88, vcc
	v_cmp_le_u32_e32 vcc, v96, v207
	v_subrev_u32_e32 v96, 42, v65
	s_nop 0
	v_cndmask_b32_e32 v56, v252, v56, vcc
	v_cmp_le_u32_e32 vcc, v96, v207
	v_add_u32_e32 v96, -10, v65
	s_nop 0
	v_cndmask_b32_e32 v89, v252, v89, vcc
	v_cmp_le_u32_e32 vcc, v96, v207
	v_subrev_u32_e32 v96, 41, v65
	s_nop 0
	v_cndmask_b32_e32 v57, v252, v57, vcc
	v_cmp_le_u32_e32 vcc, v96, v207
	v_add_u32_e32 v96, -9, v65
	s_nop 0
	v_cndmask_b32_e32 v90, v252, v90, vcc
	v_cmp_le_u32_e32 vcc, v96, v207
	v_subrev_u32_e32 v96, 40, v65
	s_nop 0
	v_cndmask_b32_e32 v58, v252, v58, vcc
	v_cmp_le_u32_e32 vcc, v96, v207
	v_add_u32_e32 v96, -8, v65
	s_nop 0
	v_cndmask_b32_e32 v91, v252, v91, vcc
	v_cmp_le_u32_e32 vcc, v96, v207
	v_subrev_u32_e32 v96, 35, v65
	s_nop 0
	v_cndmask_b32_e32 v59, v252, v59, vcc
	v_cmp_le_u32_e32 vcc, v96, v207
	v_add_u32_e32 v96, -3, v65
	s_nop 0
	v_cndmask_b32_e32 v92, v252, v92, vcc
	v_cmp_le_u32_e32 vcc, v96, v207
	v_subrev_u32_e32 v96, 34, v65
	s_nop 0
	v_cndmask_b32_e32 v60, v252, v60, vcc
	v_cmp_le_u32_e32 vcc, v96, v207
	v_add_u32_e32 v96, -2, v65
	s_nop 0
	v_cndmask_b32_e32 v93, v252, v93, vcc
	v_cmp_le_u32_e32 vcc, v96, v207
	v_subrev_u32_e32 v96, 33, v65
	s_nop 0
	v_cndmask_b32_e32 v61, v252, v61, vcc
	v_cmp_le_u32_e32 vcc, v96, v207
	v_add_u32_e32 v96, -1, v65
	s_nop 0
	v_cndmask_b32_e32 v94, v252, v94, vcc
	v_cmp_le_u32_e32 vcc, v96, v207
	v_subrev_u32_e32 v96, 32, v65
	s_nop 0
	v_cndmask_b32_e32 v62, v252, v62, vcc
	v_cmp_le_u32_e32 vcc, v96, v207
	s_nop 1
	v_cndmask_b32_e32 v95, v252, v95, vcc
	v_cmp_le_u32_e32 vcc, v65, v207
	s_nop 1
	v_cndmask_b32_e32 v63, v252, v63, vcc

.Lmfill_0a:
	s_nop 7
	s_nop 4
	v_mov_b32_e32 v82, v205
	v_mov_b32_e32 v99, v205
	v_mov_b32_e32 v98, v205
	v_mov_b32_e32 v83, v205
	v_mov_b32_e32 v100, v205
	v_mov_b32_e32 v84, v205
	v_mov_b32_e32 v101, v205
	v_mov_b32_e32 v85, v205
	v_mov_b32_e32 v102, v205
	v_mov_b32_e32 v86, v205
	v_mov_b32_e32 v103, v205
	v_mov_b32_e32 v87, v205
	v_mov_b32_e32 v104, v205
	v_mov_b32_e32 v88, v205
	v_mov_b32_e32 v105, v205
	v_mov_b32_e32 v89, v205
	v_mov_b32_e32 v106, v205
	v_mov_b32_e32 v90, v205
	v_mov_b32_e32 v107, v205
	v_mov_b32_e32 v91, v205
	v_mov_b32_e32 v108, v205
	v_mov_b32_e32 v92, v205
	v_mov_b32_e32 v109, v205
	v_mov_b32_e32 v93, v205
	v_mov_b32_e32 v110, v205
	v_mov_b32_e32 v94, v205
	v_mov_b32_e32 v111, v205
	v_mov_b32_e32 v95, v205
	v_mov_b32_e32 v112, v205
	v_mov_b32_e32 v96, v205
	v_mov_b32_e32 v113, v205
	v_mov_b32_e32 v97, v205
	s_branch .LBB1_29
.Lmfill_0b:
	s_nop 7
	s_nop 4
	v_mov_b32_e32 v50, v205
	v_mov_b32_e32 v67, v205
	v_mov_b32_e32 v66, v205
	v_mov_b32_e32 v51, v205
	v_mov_b32_e32 v68, v205
	v_mov_b32_e32 v52, v205
	v_mov_b32_e32 v69, v205
	v_mov_b32_e32 v53, v205
	v_mov_b32_e32 v70, v205
	v_mov_b32_e32 v54, v205
	v_mov_b32_e32 v71, v205
	v_mov_b32_e32 v55, v205
	v_mov_b32_e32 v72, v205
	v_mov_b32_e32 v56, v205
	v_mov_b32_e32 v73, v205
	v_mov_b32_e32 v57, v205
	v_mov_b32_e32 v74, v205
	v_mov_b32_e32 v58, v205
	v_mov_b32_e32 v75, v205
	v_mov_b32_e32 v59, v205
	v_mov_b32_e32 v76, v205
	v_mov_b32_e32 v60, v205
	v_mov_b32_e32 v77, v205
	v_mov_b32_e32 v61, v205
	v_mov_b32_e32 v78, v205
	v_mov_b32_e32 v62, v205
	v_mov_b32_e32 v79, v205
	v_mov_b32_e32 v63, v205
	v_mov_b32_e32 v80, v205
	v_mov_b32_e32 v64, v205
	v_mov_b32_e32 v81, v205
	v_mov_b32_e32 v65, v205
	s_branch .LBB1_40
.Lmfill_0f:
	s_nop 7
	s_nop 4
	v_or_b32_e32 v214, 0xe0, v210
	v_or_b32_e32 v213, 0xc0, v210
	v_mov_b32_e32 v67, 0xff800000
	v_or_b32_e32 v215, 0xe1, v210
	v_or_b32_e32 v216, 0xc2, v210
	v_mov_b32_e32 v34, v67
	v_or_b32_e32 v217, 0xe2, v210
	v_or_b32_e32 v218, 0xc3, v210
	v_mov_b32_e32 v51, v67
	v_or_b32_e32 v219, 0xe3, v210
	v_or_b32_e32 v220, 0xc8, v210
	v_mov_b32_e32 v50, v67
	v_or_b32_e32 v221, 0xe8, v210
	v_or_b32_e32 v222, 0xc9, v210
	v_mov_b32_e32 v35, v67
	v_or_b32_e32 v223, 0xe9, v210
	v_or_b32_e32 v224, 0xca, v210
	v_mov_b32_e32 v52, v67
	v_or_b32_e32 v225, 0xea, v210
	v_or_b32_e32 v226, 0xcb, v210
	v_mov_b32_e32 v36, v67
	v_or_b32_e32 v227, 0xeb, v210
	v_or_b32_e32 v228, 0xd0, v210
	v_mov_b32_e32 v53, v67
	v_or_b32_e32 v229, 0xf0, v210
	v_or_b32_e32 v230, 0xd1, v210
	v_mov_b32_e32 v37, v67
	v_or_b32_e32 v231, 0xf1, v210
	v_or_b32_e32 v232, 0xd2, v210
	v_mov_b32_e32 v54, v67
	v_or_b32_e32 v233, 0xf2, v210
	v_or_b32_e32 v234, 0xd3, v210
	v_mov_b32_e32 v38, v67
	v_or_b32_e32 v235, 0xf3, v210
	v_or_b32_e32 v236, 0xd8, v210
	v_mov_b32_e32 v55, v67
	v_or_b32_e32 v237, 0xf8, v210
	v_or_b32_e32 v238, 0xd9, v210
	v_mov_b32_e32 v39, v67
	v_or_b32_e32 v239, 0xf9, v210
	v_or_b32_e32 v240, 0xda, v210
	v_mov_b32_e32 v56, v67
	v_or_b32_e32 v241, 0xfa, v210
	v_or_b32_e32 v242, 0xdb, v210
	v_mov_b32_e32 v40, v67
	v_or_b32_e32 v243, 0xfb, v210
	v_max_f32_e32 v68, v50, v50
	v_mov_b32_e32 v57, v67
	v_add_f32_e32 v82, v203, v66
	s_mov_b32 s2, 0x41000000
	v_mov_b32_e32 v41, v67
	v_mov_b32_e32 v58, v67
	v_mov_b32_e32 v42, v67
	v_mov_b32_e32 v59, v67
	v_mov_b32_e32 v43, v67
	v_mov_b32_e32 v60, v67
	v_mov_b32_e32 v44, v67
	v_mov_b32_e32 v61, v67
	v_mov_b32_e32 v45, v67
	v_mov_b32_e32 v62, v67
	v_mov_b32_e32 v46, v67
	v_mov_b32_e32 v63, v67
	v_mov_b32_e32 v47, v67
	v_mov_b32_e32 v64, v67
	v_mov_b32_e32 v48, v67
	v_mov_b32_e32 v65, v67
	v_mov_b32_e32 v49, v67
	s_branch .Lmend_0f
.Lmfill_1f:
	s_nop 7
	s_nop 4
	v_mov_b32_e32 v66, 0xff800000
	s_mov_b32 s2, 0x41000000
	v_mov_b32_e32 v32, v66
	v_mov_b32_e32 v49, v66
	v_mov_b32_e32 v48, v66
	v_max_f32_e32 v67, v48, v48
	v_add_f32_e32 v96, v64, v65
	v_mov_b32_e32 v33, v66
	v_mov_b32_e32 v50, v66
	v_mov_b32_e32 v34, v66
	v_mov_b32_e32 v51, v66
	v_mov_b32_e32 v35, v66
	v_mov_b32_e32 v52, v66
	v_mov_b32_e32 v36, v66
	v_mov_b32_e32 v53, v66
	v_mov_b32_e32 v37, v66
	v_mov_b32_e32 v54, v66
	v_mov_b32_e32 v38, v66
	v_mov_b32_e32 v55, v66
	v_mov_b32_e32 v39, v66
	v_mov_b32_e32 v56, v66
	v_mov_b32_e32 v40, v66
	v_mov_b32_e32 v57, v66
	v_mov_b32_e32 v41, v66
	v_mov_b32_e32 v58, v66
	v_mov_b32_e32 v42, v66
	v_mov_b32_e32 v59, v66
	v_mov_b32_e32 v43, v66
	v_mov_b32_e32 v60, v66
	v_mov_b32_e32 v44, v66
	v_mov_b32_e32 v61, v66
	v_mov_b32_e32 v45, v66
	v_mov_b32_e32 v62, v66
	v_mov_b32_e32 v46, v66
	v_mov_b32_e32 v63, v66
	v_mov_b32_e32 v47, v66
	s_branch .Lmend_1f
.Lmfill_1a:
	s_nop 7
	s_nop 4
	v_mov_b32_e32 v96, v252
	v_mov_b32_e32 v113, v252
	v_mov_b32_e32 v112, v252
	v_mov_b32_e32 v97, v252
	v_mov_b32_e32 v114, v252
	v_mov_b32_e32 v98, v252
	v_mov_b32_e32 v115, v252
	v_mov_b32_e32 v99, v252
	v_mov_b32_e32 v116, v252
	v_mov_b32_e32 v100, v252
	v_mov_b32_e32 v117, v252
	v_mov_b32_e32 v101, v252
	v_mov_b32_e32 v118, v252
	v_mov_b32_e32 v102, v252
	v_mov_b32_e32 v119, v252
	v_mov_b32_e32 v103, v252
	v_mov_b32_e32 v120, v252
	v_mov_b32_e32 v104, v252
	v_mov_b32_e32 v121, v252
	v_mov_b32_e32 v105, v252
	v_mov_b32_e32 v122, v252
	v_mov_b32_e32 v106, v252
	v_mov_b32_e32 v123, v252
	v_mov_b32_e32 v107, v252
	v_mov_b32_e32 v124, v252
	v_mov_b32_e32 v108, v252
	v_mov_b32_e32 v125, v252
	v_mov_b32_e32 v109, v252
	v_mov_b32_e32 v126, v252
	v_mov_b32_e32 v110, v252
	v_mov_b32_e32 v127, v252
	v_mov_b32_e32 v111, v252
	s_branch .LBB1_116
.Lmfill_1b:
	s_nop 7
	s_nop 4
	v_mov_b32_e32 v48, v252
	v_mov_b32_e32 v81, v252
	v_mov_b32_e32 v80, v252
	v_mov_b32_e32 v49, v252
	v_mov_b32_e32 v82, v252
	v_mov_b32_e32 v50, v252
	v_mov_b32_e32 v83, v252
	v_mov_b32_e32 v51, v252
	v_mov_b32_e32 v84, v252
	v_mov_b32_e32 v52, v252
	v_mov_b32_e32 v85, v252
	v_mov_b32_e32 v53, v252
	v_mov_b32_e32 v86, v252
	v_mov_b32_e32 v54, v252
	v_mov_b32_e32 v87, v252
	v_mov_b32_e32 v55, v252
	v_mov_b32_e32 v88, v252
	v_mov_b32_e32 v56, v252
	v_mov_b32_e32 v89, v252
	v_mov_b32_e32 v57, v252
	v_mov_b32_e32 v90, v252
	v_mov_b32_e32 v58, v252
	v_mov_b32_e32 v91, v252
	v_mov_b32_e32 v59, v252
	v_mov_b32_e32 v92, v252
	v_mov_b32_e32 v60, v252
	v_mov_b32_e32 v93, v252
	v_mov_b32_e32 v61, v252
	v_mov_b32_e32 v94, v252
	v_mov_b32_e32 v62, v252
	v_mov_b32_e32 v95, v252
	v_mov_b32_e32 v63, v252
	s_branch .LBB1_127
	.p2align	8
